# attention: skip the accumulator rescale while every running max is still the sentinel (first key tile: accumulator is zero); on top of prefetch + finalize + no-copy
# baseline (speedup 1.0000x reference)
.LBB0_730:
	s_nop 6
	v_max_f32_e32 v66, v131, v131
	v_max_f32_e32 v67, v130, v130
	v_max_f32_e32 v66, v67, v66
	v_max3_f32 v66, v66, v132, v133
	v_max3_f32 v66, v66, v134, v135
	v_max3_f32 v66, v66, v136, v137
	v_and_b32_e32 v68, 64, v166
	v_max3_f32 v66, v66, v138, v139
	v_xor_b32_e32 v67, 32, v166
	v_add_u32_e32 v68, 64, v68
	v_max3_f32 v66, v66, v140, v141
	v_cmp_lt_i32_e32 vcc, v67, v68
	v_max3_f32 v66, v66, v142, v143
	v_max3_f32 v66, v66, v144, v145
	v_cndmask_b32_e32 v67, v166, v67, vcc
	v_lshlrev_b32_e32 v67, 2, v67
	ds_bpermute_b32 v67, v67, v66
	s_waitcnt lgkmcnt(0)
	v_add3_u32 v70, v69, v185, v194
	ds_read_b64_tr_b16 v[114:115], v70 offset:8192
	v_add3_u32 v71, v69, v187, v195
	ds_read_b64_tr_b16 v[116:117], v71 offset:8192
	v_add3_u32 v70, v69, v185, v197
	ds_read_b64_tr_b16 v[118:119], v70 offset:8192
	v_add3_u32 v71, v69, v187, v198
	ds_read_b64_tr_b16 v[120:121], v71 offset:8192
	v_add3_u32 v70, v69, v184, v194
	ds_read_b64_tr_b16 v[122:123], v70 offset:8192
	v_add3_u32 v71, v69, v189, v196
	ds_read_b64_tr_b16 v[124:125], v71 offset:8192
	v_add3_u32 v70, v69, v184, v197
	ds_read_b64_tr_b16 v[126:127], v70 offset:8192
	v_add3_u32 v71, v69, v189, v199
	ds_read_b64_tr_b16 v[128:129], v71 offset:8192
	v_max_f32_e32 v67, v67, v67
	v_max_f32_e32 v66, v66, v67
	v_add_f32_e32 v67, 0x40c00000, v231
	v_cmp_gt_f32_e32 vcc, v66, v67
	s_nop 1
	v_cndmask_b32_e32 v233, v231, v66, vcc
	v_sub_f32_e32 v66, v231, v233
	v_exp_f32_e32 v146, v66
	s_cbranch_vccz .LBB0_732
	v_cmp_ne_u32_e32 vcc, 0xf149f2ca, v231
	s_cbranch_vccz .LBB0_732
	v_pk_mul_f32 v[64:65], v[64:65], v[146:147] op_sel_hi:[1,0]
	v_pk_mul_f32 v[62:63], v[62:63], v[146:147] op_sel_hi:[1,0]
	v_pk_mul_f32 v[60:61], v[60:61], v[146:147] op_sel_hi:[1,0]
	v_pk_mul_f32 v[58:59], v[58:59], v[146:147] op_sel_hi:[1,0]
	v_pk_mul_f32 v[56:57], v[56:57], v[146:147] op_sel_hi:[1,0]
	v_pk_mul_f32 v[54:55], v[54:55], v[146:147] op_sel_hi:[1,0]
	v_pk_mul_f32 v[52:53], v[52:53], v[146:147] op_sel_hi:[1,0]
	v_pk_mul_f32 v[50:51], v[50:51], v[146:147] op_sel_hi:[1,0]
	v_pk_mul_f32 v[48:49], v[48:49], v[146:147] op_sel_hi:[1,0]
	v_pk_mul_f32 v[46:47], v[46:47], v[146:147] op_sel_hi:[1,0]
	v_pk_mul_f32 v[44:45], v[44:45], v[146:147] op_sel_hi:[1,0]
	v_pk_mul_f32 v[42:43], v[42:43], v[146:147] op_sel_hi:[1,0]
	v_pk_mul_f32 v[40:41], v[40:41], v[146:147] op_sel_hi:[1,0]
	v_pk_mul_f32 v[38:39], v[38:39], v[146:147] op_sel_hi:[1,0]
	v_pk_mul_f32 v[36:37], v[36:37], v[146:147] op_sel_hi:[1,0]
	v_pk_mul_f32 v[34:35], v[34:35], v[146:147] op_sel_hi:[1,0]
	v_pk_mul_f32 v[32:33], v[32:33], v[146:147] op_sel_hi:[1,0]
	v_pk_mul_f32 v[30:31], v[30:31], v[146:147] op_sel_hi:[1,0]
	v_pk_mul_f32 v[28:29], v[28:29], v[146:147] op_sel_hi:[1,0]
	v_pk_mul_f32 v[26:27], v[26:27], v[146:147] op_sel_hi:[1,0]
	v_pk_mul_f32 v[24:25], v[24:25], v[146:147] op_sel_hi:[1,0]
	v_pk_mul_f32 v[22:23], v[22:23], v[146:147] op_sel_hi:[1,0]
	v_pk_mul_f32 v[20:21], v[20:21], v[146:147] op_sel_hi:[1,0]
	v_pk_mul_f32 v[18:19], v[18:19], v[146:147] op_sel_hi:[1,0]
	v_pk_mul_f32 v[16:17], v[16:17], v[146:147] op_sel_hi:[1,0]
	v_pk_mul_f32 v[14:15], v[14:15], v[146:147] op_sel_hi:[1,0]
	v_pk_mul_f32 v[12:13], v[12:13], v[146:147] op_sel_hi:[1,0]
	v_pk_mul_f32 v[10:11], v[10:11], v[146:147] op_sel_hi:[1,0]
	v_pk_mul_f32 v[8:9], v[8:9], v[146:147] op_sel_hi:[1,0]
	v_pk_mul_f32 v[6:7], v[6:7], v[146:147] op_sel_hi:[1,0]
	v_pk_mul_f32 v[4:5], v[4:5], v[146:147] op_sel_hi:[1,0]
	v_pk_mul_f32 v[2:3], v[2:3], v[146:147] op_sel_hi:[1,0]
	s_branch .LBB0_733

.LBB0_800:
	s_nop 6
	v_max_f32_e32 v66, v131, v131
	v_max_f32_e32 v67, v130, v130
	v_max_f32_e32 v66, v67, v66
	v_max3_f32 v66, v66, v132, v133
	v_max3_f32 v66, v66, v134, v135
	v_max3_f32 v66, v66, v136, v137
	v_and_b32_e32 v68, 64, v166
	v_max3_f32 v66, v66, v138, v139
	v_xor_b32_e32 v67, 32, v166
	v_add_u32_e32 v68, 64, v68
	v_max3_f32 v66, v66, v140, v141
	v_cmp_lt_i32_e32 vcc, v67, v68
	v_max3_f32 v66, v66, v142, v143
	v_max3_f32 v66, v66, v144, v145
	v_cndmask_b32_e32 v67, v166, v67, vcc
	v_lshlrev_b32_e32 v67, 2, v67
	ds_bpermute_b32 v67, v67, v66
	s_waitcnt lgkmcnt(0)
	v_add3_u32 v70, v69, v185, v194
	ds_read_b64_tr_b16 v[114:115], v70 offset:8192
	v_add3_u32 v71, v69, v187, v195
	ds_read_b64_tr_b16 v[116:117], v71 offset:8192
	v_add3_u32 v70, v69, v185, v197
	ds_read_b64_tr_b16 v[118:119], v70 offset:8192
	v_add3_u32 v71, v69, v187, v198
	ds_read_b64_tr_b16 v[120:121], v71 offset:8192
	v_add3_u32 v70, v69, v184, v194
	ds_read_b64_tr_b16 v[122:123], v70 offset:8192
	v_add3_u32 v71, v69, v189, v196
	ds_read_b64_tr_b16 v[124:125], v71 offset:8192
	v_add3_u32 v70, v69, v184, v197
	ds_read_b64_tr_b16 v[126:127], v70 offset:8192
	v_add3_u32 v71, v69, v189, v199
	ds_read_b64_tr_b16 v[128:129], v71 offset:8192
	v_max_f32_e32 v67, v67, v67
	v_max_f32_e32 v66, v66, v67
	v_add_f32_e32 v67, 0x40c00000, v233
	v_cmp_gt_f32_e32 vcc, v66, v67
	s_nop 1
	v_cndmask_b32_e32 v235, v233, v66, vcc
	v_sub_f32_e32 v66, v233, v235
	v_exp_f32_e32 v146, v66
	s_cbranch_vccz .LBB0_802
	v_cmp_ne_u32_e32 vcc, 0xf149f2ca, v233
	s_cbranch_vccz .LBB0_802
	v_pk_mul_f32 v[64:65], v[64:65], v[146:147] op_sel_hi:[1,0]
	v_pk_mul_f32 v[62:63], v[62:63], v[146:147] op_sel_hi:[1,0]
	v_pk_mul_f32 v[60:61], v[60:61], v[146:147] op_sel_hi:[1,0]
	v_pk_mul_f32 v[58:59], v[58:59], v[146:147] op_sel_hi:[1,0]
	v_pk_mul_f32 v[56:57], v[56:57], v[146:147] op_sel_hi:[1,0]
	v_pk_mul_f32 v[54:55], v[54:55], v[146:147] op_sel_hi:[1,0]
	v_pk_mul_f32 v[52:53], v[52:53], v[146:147] op_sel_hi:[1,0]
	v_pk_mul_f32 v[50:51], v[50:51], v[146:147] op_sel_hi:[1,0]
	v_pk_mul_f32 v[48:49], v[48:49], v[146:147] op_sel_hi:[1,0]
	v_pk_mul_f32 v[46:47], v[46:47], v[146:147] op_sel_hi:[1,0]
	v_pk_mul_f32 v[44:45], v[44:45], v[146:147] op_sel_hi:[1,0]
	v_pk_mul_f32 v[42:43], v[42:43], v[146:147] op_sel_hi:[1,0]
	v_pk_mul_f32 v[40:41], v[40:41], v[146:147] op_sel_hi:[1,0]
	v_pk_mul_f32 v[38:39], v[38:39], v[146:147] op_sel_hi:[1,0]
	v_pk_mul_f32 v[36:37], v[36:37], v[146:147] op_sel_hi:[1,0]
	v_pk_mul_f32 v[34:35], v[34:35], v[146:147] op_sel_hi:[1,0]
	v_pk_mul_f32 v[32:33], v[32:33], v[146:147] op_sel_hi:[1,0]
	v_pk_mul_f32 v[30:31], v[30:31], v[146:147] op_sel_hi:[1,0]
	v_pk_mul_f32 v[28:29], v[28:29], v[146:147] op_sel_hi:[1,0]
	v_pk_mul_f32 v[26:27], v[26:27], v[146:147] op_sel_hi:[1,0]
	v_pk_mul_f32 v[24:25], v[24:25], v[146:147] op_sel_hi:[1,0]
	v_pk_mul_f32 v[22:23], v[22:23], v[146:147] op_sel_hi:[1,0]
	v_pk_mul_f32 v[20:21], v[20:21], v[146:147] op_sel_hi:[1,0]
	v_pk_mul_f32 v[18:19], v[18:19], v[146:147] op_sel_hi:[1,0]
	v_pk_mul_f32 v[16:17], v[16:17], v[146:147] op_sel_hi:[1,0]
	v_pk_mul_f32 v[14:15], v[14:15], v[146:147] op_sel_hi:[1,0]
	v_pk_mul_f32 v[12:13], v[12:13], v[146:147] op_sel_hi:[1,0]
	v_pk_mul_f32 v[10:11], v[10:11], v[146:147] op_sel_hi:[1,0]
	v_pk_mul_f32 v[8:9], v[8:9], v[146:147] op_sel_hi:[1,0]
	v_pk_mul_f32 v[6:7], v[6:7], v[146:147] op_sel_hi:[1,0]
	v_pk_mul_f32 v[4:5], v[4:5], v[146:147] op_sel_hi:[1,0]
	v_pk_mul_f32 v[2:3], v[2:3], v[146:147] op_sel_hi:[1,0]
	s_branch .LBB0_803
